# o8stage: differential-attention unit epilogue output bytes staged through a per-wave 4 KB LDS image and stored as 4 dwordx4 per lane (8 full 128-B row segments per instruction) instead of 64 one-byte
# speedup vs baseline: 1.0021x; 1.0005x over previous
.LBB0_1202:
	s_nop 15
	v_add_f32_e32 v248, v18, v19
	v_add_f32_e32 v249, v20, v21
	v_add_f32_e32 v248, v248, v249
	v_cmp_u_f32_e64 s[100:101], v248, v248
	s_nop 1
	s_cmp_lg_u64 s[100:101], 0
	s_cselect_b32 s100, 1, 0
	s_or_b32 s99, s99, s100
	s_mov_b64 s[100:101], exec
	s_mov_b32 exec_lo, 0x30003
	s_mov_b32 exec_hi, 0x30003
	ds_write_b128 v250, v[18:21] offset:49152
	s_mov_b64 exec, s[100:101]
	v_add_u32_e32 v249, s78, v186
	v_mov_b32_e32 v248, s78
	v_mov_b32_e32 v251, s99
	ds_write_b32 v248, v251 offset:49404
	s_waitcnt lgkmcnt(0)
	ds_read_b128 v[30:33], v249 offset:49248
	ds_read_b128 v[26:29], v249 offset:49216
	ds_read_b128 v[22:25], v249 offset:49184
	ds_read_b128 v[18:21], v249 offset:49152
	s_waitcnt lgkmcnt(0)
	v_rcp_f32_e32 v18, v18
	v_rcp_f32_e32 v19, v19
	v_mov_b32_e32 v92, v179
	s_waitcnt vmcnt(0) lgkmcnt(0)
	s_barrier
	v_and_b32_e32 v248, 7, v193
	v_lshlrev_b32_e32 v248, 8, v248
	ds_read_b32 v251, v248 offset:49404
	s_waitcnt lgkmcnt(0)
	v_cmp_ne_u32_e64 s[100:101], 0, v251
	s_nop 1
	s_cmp_lg_u64 s[100:101], 0
	s_cselect_b32 s99, 1, 0
	v_mul_f32_e32 v2, v2, v18
	v_mul_f32_e32 v34, v34, v18
	v_mul_f32_e32 v50, v50, v18
	v_mul_f32_e32 v82, v66, v18
	v_mul_f32_e32 v18, v3, v19
	v_rcp_f32_e32 v3, v20
	v_mul_f32_e32 v35, v35, v19
	v_mul_f32_e32 v83, v51, v19
	v_mul_f32_e32 v19, v67, v19
	v_mul_f32_e32 v20, v4, v3
	v_rcp_f32_e32 v4, v21
	v_mul_f32_e32 v21, v36, v3
	v_mul_f32_e32 v52, v52, v3
	v_mul_f32_e32 v67, v68, v3
	v_rcp_f32_e32 v3, v22
	v_mul_f32_e32 v36, v5, v4
	v_mul_f32_e32 v22, v37, v4
	v_mul_f32_e32 v84, v53, v4
	v_mul_f32_e32 v85, v69, v4
	v_rcp_f32_e32 v4, v23
	v_mul_f32_e32 v37, v6, v3
	v_mul_f32_e32 v23, v38, v3
	v_mul_f32_e32 v38, v54, v3
	v_mul_f32_e32 v70, v70, v3
	v_rcp_f32_e32 v3, v24
	v_mul_f32_e32 v51, v7, v4
	v_mul_f32_e32 v39, v39, v4
	v_mul_f32_e32 v54, v55, v4
	v_mul_f32_e32 v55, v71, v4
	v_rcp_f32_e32 v4, v25
	v_mul_f32_e32 v8, v8, v3
	v_mul_f32_e32 v25, v40, v3
	v_mul_f32_e32 v40, v56, v3
	v_mul_f32_e32 v72, v72, v3
	v_rcp_f32_e32 v3, v26
	v_mul_f32_e32 v9, v9, v4
	v_mul_f32_e32 v26, v41, v4
	v_mul_f32_e32 v57, v57, v4
	v_mul_f32_e32 v86, v73, v4
	v_rcp_f32_e32 v4, v27
	v_mul_f32_e32 v10, v10, v3
	v_mul_f32_e32 v27, v42, v3
	v_mul_f32_e32 v87, v58, v3
	v_mul_f32_e32 v88, v74, v3
	v_rcp_f32_e32 v3, v28
	v_mul_f32_e32 v11, v11, v4
	v_mul_f32_e32 v43, v43, v4
	v_mul_f32_e32 v74, v59, v4
	v_mul_f32_e32 v75, v75, v4
	v_rcp_f32_e32 v4, v29
	v_mul_f32_e32 v12, v12, v3
	v_mul_f32_e32 v44, v44, v3
	v_mul_f32_e32 v60, v60, v3
	v_mul_f32_e32 v89, v76, v3
	v_rcp_f32_e32 v3, v30
	v_mul_f32_e32 v13, v13, v4
	v_mul_f32_e32 v30, v45, v4
	v_mul_f32_e32 v45, v61, v4
	v_mul_f32_e32 v77, v77, v4
	v_rcp_f32_e32 v4, v31
	v_mul_f32_e32 v14, v14, v3
	v_mul_f32_e32 v31, v46, v3
	v_mul_f32_e32 v62, v62, v3
	v_mul_f32_e32 v78, v78, v3
	v_rcp_f32_e32 v3, v32
	v_mul_f32_e32 v15, v15, v4
	v_mul_f32_e32 v32, v47, v4
	v_mul_f32_e32 v90, v63, v4
	v_mul_f32_e32 v79, v79, v4
	ds_read2st64_b32 v[4:5], v92 offset1:8
	v_mul_f32_e32 v29, v16, v3
	v_mul_f32_e32 v48, v48, v3
	v_mul_f32_e32 v91, v64, v3
	v_mul_f32_e32 v80, v80, v3
	v_rcp_f32_e32 v3, v33
	ds_read2st64_b32 v[6:7], v92 offset0:16 offset1:24
	v_mul_f32_e32 v17, v17, v3
	v_mul_f32_e32 v33, v49, v3
	v_mul_f32_e32 v65, v65, v3
	v_mul_f32_e32 v81, v81, v3
	s_waitcnt lgkmcnt(0)
	v_lshlrev_b32_e32 v3, 16, v4
	v_fma_f32 v3, -v1, v2, v3
	v_and_b32_e32 v2, 0xffff0000, v4
	v_fma_f32 v68, -v1, v18, v2
	v_lshlrev_b32_e32 v2, 16, v5
	v_fma_f32 v63, -v1, v20, v2
	v_and_b32_e32 v2, 0xffff0000, v5
	ds_read2st64_b32 v[4:5], v92 offset0:32 offset1:40
	v_fma_f32 v58, -v1, v36, v2
	v_lshlrev_b32_e32 v2, 16, v6
	v_fma_f32 v53, -v1, v37, v2
	v_and_b32_e32 v2, 0xffff0000, v6
	v_fma_f32 v47, -v1, v51, v2
	v_lshlrev_b32_e32 v2, 16, v7
	v_fma_f32 v42, -v1, v8, v2
	v_and_b32_e32 v2, 0xffff0000, v7
	v_fma_f32 v36, -v1, v9, v2
	s_waitcnt lgkmcnt(0)
	v_lshlrev_b32_e32 v2, 16, v4
	v_fma_f32 v28, -v1, v10, v2
	v_and_b32_e32 v2, 0xffff0000, v4
	v_fma_f32 v24, -v1, v11, v2
	ds_read2st64_b32 v[10:11], v92 offset0:48 offset1:56
	v_lshlrev_b32_e32 v2, 16, v5
	v_fma_f32 v20, -v1, v12, v2
	v_and_b32_e32 v2, 0xffff0000, v5
	ds_read2st64_b32 v[4:5], v92 offset0:64 offset1:72
	v_fma_f32 v16, -v1, v13, v2
	s_waitcnt lgkmcnt(0)
	v_lshlrev_b32_e32 v2, 16, v10
	v_fma_f32 v12, -v1, v14, v2
	v_and_b32_e32 v2, 0xffff0000, v10
	v_fma_f32 v9, -v1, v15, v2
	v_lshlrev_b32_e32 v2, 16, v11
	v_fma_f32 v7, -v1, v29, v2
	v_and_b32_e32 v2, 0xffff0000, v11
	v_fma_f32 v6, -v1, v17, v2
	v_lshlrev_b32_e32 v2, 16, v4
	v_fma_f32 v76, -v1, v34, v2
	v_and_b32_e32 v2, 0xffff0000, v4
	v_lshlrev_b32_e32 v4, 16, v5
	v_fma_f32 v66, -v1, v21, v4
	v_and_b32_e32 v4, 0xffff0000, v5
	v_fma_f32 v61, -v1, v22, v4
	ds_read2st64_b32 v[4:5], v92 offset0:80 offset1:88
	ds_read2st64_b32 v[14:15], v92 offset0:144 offset1:152
	v_fma_f32 v71, -v1, v35, v2
	v_mul_f32_e32 v2, v76, v76
	v_fmac_f32_e32 v2, v3, v3
	s_waitcnt lgkmcnt(0)
	v_lshlrev_b32_e32 v8, 16, v4
	v_and_b32_e32 v4, 0xffff0000, v4
	v_fma_f32 v51, -v1, v39, v4
	v_lshlrev_b32_e32 v4, 16, v5
	v_fma_f32 v46, -v1, v25, v4
	v_and_b32_e32 v4, 0xffff0000, v5
	v_fma_f32 v41, -v1, v26, v4
	ds_read2st64_b32 v[4:5], v92 offset0:96 offset1:104
	v_fma_f32 v56, -v1, v23, v8
	v_mul_f32_e32 v34, v71, v71
	v_fmac_f32_e32 v34, v68, v68
	v_mul_f32_e32 v93, v66, v66
	s_waitcnt lgkmcnt(0)
	v_lshlrev_b32_e32 v8, 16, v4
	v_and_b32_e32 v4, 0xffff0000, v4
	v_fma_f32 v29, -v1, v43, v4
	v_lshlrev_b32_e32 v4, 16, v5
	v_fma_f32 v25, -v1, v44, v4
	v_and_b32_e32 v4, 0xffff0000, v5
	v_fma_f32 v21, -v1, v30, v4
	ds_read2st64_b32 v[4:5], v92 offset0:112 offset1:120
	v_fma_f32 v37, -v1, v27, v8
	v_fmac_f32_e32 v93, v63, v63
	v_mul_f32_e32 v94, v61, v61
	v_fmac_f32_e32 v94, v58, v58
	s_waitcnt lgkmcnt(0)
	v_lshlrev_b32_e32 v8, 16, v4
	v_and_b32_e32 v4, 0xffff0000, v4
	v_fma_f32 v13, -v1, v32, v4
	v_lshlrev_b32_e32 v4, 16, v5
	v_fma_f32 v10, -v1, v48, v4
	v_and_b32_e32 v4, 0xffff0000, v5
	v_fma_f32 v17, -v1, v31, v8
	v_fma_f32 v8, -v1, v33, v4
	ds_read2st64_b32 v[4:5], v92 offset0:128 offset1:136
	ds_read2st64_b32 v[30:31], v92 offset0:208 offset1:216
	v_mul_f32_e32 v95, v56, v56
	v_fmac_f32_e32 v95, v53, v53
	v_mul_f32_e32 v96, v51, v51
	s_waitcnt lgkmcnt(0)
	v_lshlrev_b32_e32 v11, 16, v4
	v_and_b32_e32 v4, 0xffff0000, v4
	v_fma_f32 v83, -v1, v83, v4
	v_lshlrev_b32_e32 v4, 16, v5
	v_fma_f32 v73, -v1, v52, v4
	v_and_b32_e32 v4, 0xffff0000, v5
	v_fma_f32 v69, -v1, v84, v4
	v_lshlrev_b32_e32 v4, 16, v14
	v_fma_f32 v64, -v1, v38, v4
	v_and_b32_e32 v4, 0xffff0000, v14
	v_fma_f32 v59, -v1, v54, v4
	v_lshlrev_b32_e32 v4, 16, v15
	v_fma_f32 v54, -v1, v40, v4
	ds_read2st64_b32 v[4:5], v92 offset0:160 offset1:168
	v_fma_f32 v105, -v1, v50, v11
	v_and_b32_e32 v11, 0xffff0000, v15
	ds_read2st64_b32 v[14:15], v92 offset0:176 offset1:184
	v_fma_f32 v49, -v1, v57, v11
	s_waitcnt lgkmcnt(0)
	v_lshlrev_b32_e32 v11, 16, v4
	v_and_b32_e32 v4, 0xffff0000, v4
	v_fma_f32 v39, -v1, v74, v4
	v_lshlrev_b32_e32 v4, 16, v5
	v_fma_f32 v33, -v1, v60, v4
	v_and_b32_e32 v4, 0xffff0000, v5
	v_fma_f32 v26, -v1, v45, v4
	v_lshlrev_b32_e32 v4, 16, v14
	v_fma_f32 v22, -v1, v62, v4
	v_and_b32_e32 v4, 0xffff0000, v14
	v_fma_f32 v18, -v1, v90, v4
	v_lshlrev_b32_e32 v4, 16, v15
	v_fma_f32 v14, -v1, v91, v4
	ds_read2st64_b32 v[4:5], v92 offset0:192 offset1:200
	v_fma_f32 v44, -v1, v87, v11
	v_and_b32_e32 v11, 0xffff0000, v15
	v_fma_f32 v11, -v1, v65, v11
	v_fmac_f32_e32 v2, v105, v105
	s_waitcnt lgkmcnt(0)
	v_lshlrev_b32_e32 v15, 16, v4
	v_and_b32_e32 v4, 0xffff0000, v4
	v_fma_f32 v84, -v1, v19, v4
	v_lshlrev_b32_e32 v4, 16, v5
	v_fma_f32 v87, -v1, v67, v4
	v_and_b32_e32 v4, 0xffff0000, v5
	v_fma_f32 v74, -v1, v85, v4
	v_lshlrev_b32_e32 v4, 16, v30
	v_fma_f32 v70, -v1, v70, v4
	v_and_b32_e32 v4, 0xffff0000, v30
	v_fma_f32 v65, -v1, v55, v4
	v_lshlrev_b32_e32 v4, 16, v31
	v_fma_f32 v60, -v1, v72, v4
	ds_read2st64_b32 v[4:5], v92 offset0:224 offset1:232
	v_fma_f32 v82, -v1, v82, v15
	v_and_b32_e32 v15, 0xffff0000, v31
	ds_read2st64_b32 v[30:31], v92 offset0:240 offset1:248
	v_fma_f32 v55, -v1, v86, v15
	s_waitcnt lgkmcnt(0)
	v_lshlrev_b32_e32 v15, 16, v4
	v_and_b32_e32 v4, 0xffff0000, v4
	v_fma_f32 v45, -v1, v75, v4
	v_lshlrev_b32_e32 v4, 16, v5
	v_fmac_f32_e32 v2, v82, v82
	v_fma_f32 v40, -v1, v89, v4
	v_and_b32_e32 v4, 0xffff0000, v5
	v_fma_f32 v35, -v1, v77, v4
	v_lshlrev_b32_e32 v4, 16, v30
	v_add_f32_dpp v2, v2, v2 quad_perm:[1,0,3,2] row_mask:0xf bank_mask:0xf bound_ctrl:1
	v_fma_f32 v27, -v1, v78, v4
	v_and_b32_e32 v4, 0xffff0000, v30
	v_add_f32_dpp v2, v2, v2 quad_perm:[2,3,0,1] row_mask:0xf bank_mask:0xf bound_ctrl:1
	v_fma_f32 v23, -v1, v79, v4
	v_lshlrev_b32_e32 v4, 16, v31
	v_add_f32_dpp v2, v2, v2 row_half_mirror row_mask:0xf bank_mask:0xf bound_ctrl:1
	v_fma_f32 v19, -v1, v80, v4
	v_and_b32_e32 v4, 0xffff0000, v31
	v_add_f32_dpp v2, v2, v2 row_mirror row_mask:0xf bank_mask:0xf bound_ctrl:1
	v_fmac_f32_e32 v34, v83, v83
	v_fma_f32 v50, -v1, v88, v15
	v_fma_f32 v15, -v1, v81, v4
	v_mov_b32_e32 v4, v2
	v_fmac_f32_e32 v34, v84, v84
	s_nop 0
	v_permlane16_swap_b32_e32 v2, v4
	v_add_f32_e32 v2, v2, v4
	s_nop 0
	v_add_f32_dpp v4, v34, v34 quad_perm:[1,0,3,2] row_mask:0xf bank_mask:0xf bound_ctrl:1
	v_fmac_f32_e32 v93, v73, v73
	v_fmac_f32_e32 v93, v87, v87
	v_add_f32_dpp v4, v4, v4 quad_perm:[2,3,0,1] row_mask:0xf bank_mask:0xf bound_ctrl:1
	v_fmac_f32_e32 v94, v69, v69
	v_fmac_f32_e32 v94, v74, v74
	v_add_f32_dpp v4, v4, v4 row_half_mirror row_mask:0xf bank_mask:0xf bound_ctrl:1
	v_fmac_f32_e32 v95, v64, v64
	v_fmac_f32_e32 v95, v70, v70
	v_add_f32_dpp v4, v4, v4 row_mirror row_mask:0xf bank_mask:0xf bound_ctrl:1
	v_mov_b32_e32 v5, v4
	s_nop 1
	v_permlane16_swap_b32_e32 v4, v5
	v_add_f32_e32 v77, v4, v5
	s_nop 0
	v_add_f32_dpp v4, v93, v93 quad_perm:[1,0,3,2] row_mask:0xf bank_mask:0xf bound_ctrl:1
	v_fmac_f32_e32 v96, v47, v47
	v_fmac_f32_e32 v96, v59, v59
	v_add_f32_dpp v4, v4, v4 quad_perm:[2,3,0,1] row_mask:0xf bank_mask:0xf bound_ctrl:1
	v_fmac_f32_e32 v96, v65, v65
	v_mul_f32_e32 v97, v46, v46
	v_add_f32_dpp v4, v4, v4 row_half_mirror row_mask:0xf bank_mask:0xf bound_ctrl:1
	v_fmac_f32_e32 v97, v42, v42
	v_fmac_f32_e32 v97, v54, v54
	v_add_f32_dpp v4, v4, v4 row_mirror row_mask:0xf bank_mask:0xf bound_ctrl:1
	v_mov_b32_e32 v5, v4
	s_nop 1
	v_permlane16_swap_b32_e32 v4, v5
	v_add_f32_e32 v80, v4, v5
	s_nop 0
	v_add_f32_dpp v4, v94, v94 quad_perm:[1,0,3,2] row_mask:0xf bank_mask:0xf bound_ctrl:1
	v_fmac_f32_e32 v97, v60, v60
	v_mul_f32_e32 v98, v41, v41
	v_add_f32_dpp v4, v4, v4 quad_perm:[2,3,0,1] row_mask:0xf bank_mask:0xf bound_ctrl:1
	v_fmac_f32_e32 v98, v36, v36
	v_fmac_f32_e32 v98, v49, v49
	v_add_f32_dpp v4, v4, v4 row_half_mirror row_mask:0xf bank_mask:0xf bound_ctrl:1
	v_fmac_f32_e32 v98, v55, v55
	v_mul_f32_e32 v43, v37, v37
	v_add_f32_dpp v4, v4, v4 row_mirror row_mask:0xf bank_mask:0xf bound_ctrl:1
	v_mov_b32_e32 v5, v4
	s_nop 1
	v_permlane16_swap_b32_e32 v4, v5
	v_add_f32_e32 v81, v4, v5
	s_nop 0
	v_add_f32_dpp v4, v95, v95 quad_perm:[1,0,3,2] row_mask:0xf bank_mask:0xf bound_ctrl:1
	v_fmac_f32_e32 v43, v28, v28
	v_fmac_f32_e32 v43, v44, v44
	v_add_f32_dpp v4, v4, v4 quad_perm:[2,3,0,1] row_mask:0xf bank_mask:0xf bound_ctrl:1
	v_fmac_f32_e32 v43, v50, v50
	v_mul_f32_e32 v99, v29, v29
	v_add_f32_dpp v4, v4, v4 row_half_mirror row_mask:0xf bank_mask:0xf bound_ctrl:1
	v_fmac_f32_e32 v99, v24, v24
	v_fmac_f32_e32 v99, v39, v39
	v_add_f32_dpp v4, v4, v4 row_mirror row_mask:0xf bank_mask:0xf bound_ctrl:1
	v_mov_b32_e32 v5, v4
	s_nop 1
	v_permlane16_swap_b32_e32 v4, v5
	v_add_f32_e32 v85, v4, v5
	s_nop 0
	v_add_f32_dpp v4, v96, v96 quad_perm:[1,0,3,2] row_mask:0xf bank_mask:0xf bound_ctrl:1
	v_fmac_f32_e32 v99, v45, v45
	v_mul_f32_e32 v100, v25, v25
	v_add_f32_dpp v4, v4, v4 quad_perm:[2,3,0,1] row_mask:0xf bank_mask:0xf bound_ctrl:1
	v_fmac_f32_e32 v100, v20, v20
	v_fmac_f32_e32 v100, v33, v33
	v_add_f32_dpp v4, v4, v4 row_half_mirror row_mask:0xf bank_mask:0xf bound_ctrl:1
	v_fmac_f32_e32 v100, v40, v40
	v_mul_f32_e32 v101, v21, v21
	v_add_f32_dpp v4, v4, v4 row_mirror row_mask:0xf bank_mask:0xf bound_ctrl:1
	v_mov_b32_e32 v5, v4
	s_nop 1
	v_permlane16_swap_b32_e32 v4, v5
	v_add_f32_e32 v86, v4, v5
	v_mov_b32_e32 v5, v178
	s_load_dwordx2 s[6:7], s[10:11], 0x98
	v_and_b32_e32 v180, 31, v5
	v_lshlrev_b32_e32 v30, 2, v180
	s_waitcnt lgkmcnt(0)
	global_load_dword v31, v30, s[6:7]
	global_load_dword v78, v30, s[6:7] offset:128
	global_load_dword v79, v30, s[6:7] offset:256
	s_nop 0
	global_load_dword v30, v30, s[6:7] offset:384
	v_add_f32_dpp v4, v97, v97 quad_perm:[1,0,3,2] row_mask:0xf bank_mask:0xf bound_ctrl:1
	v_fmac_f32_e32 v101, v16, v16
	v_fmac_f32_e32 v101, v26, v26
	v_add_f32_dpp v4, v4, v4 quad_perm:[2,3,0,1] row_mask:0xf bank_mask:0xf bound_ctrl:1
	v_fmac_f32_e32 v101, v35, v35
	v_mul_f32_e32 v32, v17, v17
	v_add_f32_dpp v4, v4, v4 row_half_mirror row_mask:0xf bank_mask:0xf bound_ctrl:1
	v_fmac_f32_e32 v32, v12, v12
	v_fmac_f32_e32 v32, v22, v22
	v_add_f32_dpp v4, v4, v4 row_mirror row_mask:0xf bank_mask:0xf bound_ctrl:1
	v_mov_b32_e32 v34, v4
	s_nop 1
	v_permlane16_swap_b32_e32 v4, v34
	v_add_f32_e32 v88, v4, v34
	s_nop 0
	v_add_f32_dpp v4, v98, v98 quad_perm:[1,0,3,2] row_mask:0xf bank_mask:0xf bound_ctrl:1
	v_fmac_f32_e32 v32, v27, v27
	v_mul_f32_e32 v102, v13, v13
	v_add_f32_dpp v4, v4, v4 quad_perm:[2,3,0,1] row_mask:0xf bank_mask:0xf bound_ctrl:1
	v_fmac_f32_e32 v102, v9, v9
	v_fmac_f32_e32 v102, v18, v18
	v_add_f32_dpp v4, v4, v4 row_half_mirror row_mask:0xf bank_mask:0xf bound_ctrl:1
	v_fmac_f32_e32 v102, v23, v23
	v_mul_f32_e32 v103, v10, v10
	v_add_f32_dpp v4, v4, v4 row_mirror row_mask:0xf bank_mask:0xf bound_ctrl:1
	v_mov_b32_e32 v34, v4
	s_nop 1
	v_permlane16_swap_b32_e32 v4, v34
	v_add_f32_e32 v75, v4, v34
	s_nop 0
	v_add_f32_dpp v4, v43, v43 quad_perm:[1,0,3,2] row_mask:0xf bank_mask:0xf bound_ctrl:1
	v_fmac_f32_e32 v103, v7, v7
	v_fmac_f32_e32 v103, v14, v14
	v_add_f32_dpp v4, v4, v4 quad_perm:[2,3,0,1] row_mask:0xf bank_mask:0xf bound_ctrl:1
	v_fmac_f32_e32 v103, v19, v19
	v_mul_f32_e32 v104, v8, v8
	v_add_f32_dpp v4, v4, v4 row_half_mirror row_mask:0xf bank_mask:0xf bound_ctrl:1
	v_fmac_f32_e32 v104, v6, v6
	v_fmac_f32_e32 v104, v11, v11
	v_add_f32_dpp v4, v4, v4 row_mirror row_mask:0xf bank_mask:0xf bound_ctrl:1
	v_mov_b32_e32 v34, v4
	s_nop 1
	v_permlane16_swap_b32_e32 v4, v34
	v_add_f32_e32 v72, v4, v34
	s_nop 0
	v_add_f32_dpp v4, v99, v99 quad_perm:[1,0,3,2] row_mask:0xf bank_mask:0xf bound_ctrl:1
	v_fmac_f32_e32 v104, v15, v15
	v_fmamk_f32 v2, v2, 0x3c000000, v184
	v_add_f32_dpp v4, v4, v4 quad_perm:[2,3,0,1] row_mask:0xf bank_mask:0xf bound_ctrl:1
	v_cmp_gt_f32_e32 vcc, s55, v2
	v_fmamk_f32 v77, v77, 0x3c000000, v184
	v_add_f32_dpp v4, v4, v4 row_half_mirror row_mask:0xf bank_mask:0xf bound_ctrl:1
	s_waitcnt vmcnt(0)
	v_mul_f32_e32 v30, 0x3f24fd5c, v30
	v_add_f32_dpp v4, v4, v4 row_mirror row_mask:0xf bank_mask:0xf bound_ctrl:1
	v_mov_b32_e32 v34, v4
	s_nop 1
	v_permlane16_swap_b32_e32 v4, v34
	v_add_f32_e32 v67, v4, v34
	s_nop 0
	v_add_f32_dpp v4, v100, v100 quad_perm:[1,0,3,2] row_mask:0xf bank_mask:0xf bound_ctrl:1
	s_nop 1
	v_add_f32_dpp v4, v4, v4 quad_perm:[2,3,0,1] row_mask:0xf bank_mask:0xf bound_ctrl:1
	s_nop 1
	v_add_f32_dpp v4, v4, v4 row_half_mirror row_mask:0xf bank_mask:0xf bound_ctrl:1
	s_nop 1
	v_add_f32_dpp v4, v4, v4 row_mirror row_mask:0xf bank_mask:0xf bound_ctrl:1
	v_mov_b32_e32 v34, v4
	s_nop 1
	v_permlane16_swap_b32_e32 v4, v34
	v_add_f32_e32 v62, v4, v34
	s_nop 0
	v_add_f32_dpp v4, v101, v101 quad_perm:[1,0,3,2] row_mask:0xf bank_mask:0xf bound_ctrl:1
	s_nop 1
	v_add_f32_dpp v4, v4, v4 quad_perm:[2,3,0,1] row_mask:0xf bank_mask:0xf bound_ctrl:1
	s_nop 1
	v_add_f32_dpp v4, v4, v4 row_half_mirror row_mask:0xf bank_mask:0xf bound_ctrl:1
	s_nop 1
	v_add_f32_dpp v4, v4, v4 row_mirror row_mask:0xf bank_mask:0xf bound_ctrl:1
	v_mov_b32_e32 v34, v4
	s_nop 1
	v_permlane16_swap_b32_e32 v4, v34
	v_add_f32_e32 v57, v4, v34
	s_nop 0
	v_add_f32_dpp v4, v32, v32 quad_perm:[1,0,3,2] row_mask:0xf bank_mask:0xf bound_ctrl:1
	v_mul_f32_e32 v34, 0x3f24fd5c, v31
	v_mul_f32_e32 v31, 0x3f24fd5c, v79
	v_add_f32_dpp v4, v4, v4 quad_perm:[2,3,0,1] row_mask:0xf bank_mask:0xf bound_ctrl:1
	s_nop 1
	v_add_f32_dpp v4, v4, v4 row_half_mirror row_mask:0xf bank_mask:0xf bound_ctrl:1
	s_nop 1
	v_add_f32_dpp v4, v4, v4 row_mirror row_mask:0xf bank_mask:0xf bound_ctrl:1
	v_mov_b32_e32 v32, v4
	s_nop 1
	v_permlane16_swap_b32_e32 v4, v32
	v_add_f32_e32 v52, v4, v32
	s_nop 0
	v_add_f32_dpp v4, v102, v102 quad_perm:[1,0,3,2] row_mask:0xf bank_mask:0xf bound_ctrl:1
	s_nop 1
	v_add_f32_dpp v4, v4, v4 quad_perm:[2,3,0,1] row_mask:0xf bank_mask:0xf bound_ctrl:1
	s_nop 1
	v_add_f32_dpp v4, v4, v4 row_half_mirror row_mask:0xf bank_mask:0xf bound_ctrl:1
	s_nop 1
	v_add_f32_dpp v4, v4, v4 row_mirror row_mask:0xf bank_mask:0xf bound_ctrl:1
	v_mov_b32_e32 v32, v4
	s_nop 1
	v_permlane16_swap_b32_e32 v4, v32
	v_add_f32_e32 v48, v4, v32
	s_nop 0
	v_add_f32_dpp v4, v103, v103 quad_perm:[1,0,3,2] row_mask:0xf bank_mask:0xf bound_ctrl:1
	s_nop 1
	v_add_f32_dpp v4, v4, v4 quad_perm:[2,3,0,1] row_mask:0xf bank_mask:0xf bound_ctrl:1
	s_nop 1
	v_add_f32_dpp v4, v4, v4 row_half_mirror row_mask:0xf bank_mask:0xf bound_ctrl:1
	s_nop 1
	v_add_f32_dpp v4, v4, v4 row_mirror row_mask:0xf bank_mask:0xf bound_ctrl:1
	v_mov_b32_e32 v32, v4
	s_nop 1
	v_permlane16_swap_b32_e32 v4, v32
	v_add_f32_e32 v43, v4, v32
	s_nop 0
	v_add_f32_dpp v4, v104, v104 quad_perm:[1,0,3,2] row_mask:0xf bank_mask:0xf bound_ctrl:1
	s_nop 1
	v_add_f32_dpp v4, v4, v4 quad_perm:[2,3,0,1] row_mask:0xf bank_mask:0xf bound_ctrl:1
	s_nop 1
	v_add_f32_dpp v4, v4, v4 row_half_mirror row_mask:0xf bank_mask:0xf bound_ctrl:1
	s_nop 1
	v_add_f32_dpp v4, v4, v4 row_mirror row_mask:0xf bank_mask:0xf bound_ctrl:1
	v_mov_b32_e32 v32, v4
	s_nop 1
	v_permlane16_swap_b32_e32 v4, v32
	v_add_f32_e32 v38, v4, v32
	v_mul_f32_e32 v4, 0x4f800000, v2
	v_cndmask_b32_e32 v4, v2, v4, vcc
	v_mul_f32_e32 v32, 0x3f24fd5c, v78
	v_sqrt_f32_e32 v78, v4
	v_ashrrev_i32_e32 v2, 3, v5
	v_and_b32_e32 v2, -4, v2
	v_add_u32_e32 v2, s86, v2
	v_add_u32_e32 v5, -1, v78
	v_fma_f32 v79, -v5, v78, v4
	v_cmp_ge_f32_e64 s[6:7], 0, v79
	v_add_u32_e32 v79, 1, v78
	s_nop 0
	v_cndmask_b32_e64 v5, v78, v5, s[6:7]
	v_fma_f32 v78, -v79, v78, v4
	v_cmp_lt_f32_e64 s[6:7], 0, v78
	s_nop 1
	v_cndmask_b32_e64 v5, v5, v79, s[6:7]
	v_mul_f32_e32 v78, 0x37800000, v5
	v_cndmask_b32_e32 v5, v5, v78, vcc
	v_cmp_class_f32_e32 vcc, v4, v185
	s_nop 1
	v_cndmask_b32_e32 v78, v5, v4, vcc
	v_div_scale_f32 v79, s[6:7], v78, v78, 1.0
	v_rcp_f32_e32 v89, v79
	s_add_u32 s6, s27, s87
	s_addc_u32 s7, s23, s76
	v_lshl_add_u64 v[4:5], s[6:7], 0, v[180:181]
	v_fma_f32 v90, -v79, v89, 1.0
	v_fmac_f32_e32 v89, v90, v89
	v_div_scale_f32 v90, vcc, 1.0, v78, 1.0
	v_mul_f32_e32 v91, v90, v89
	v_fma_f32 v92, -v79, v91, v90
	v_fmac_f32_e32 v91, v92, v89
	v_fma_f32 v79, -v79, v91, v90
	v_div_fmas_f32 v79, v79, v89, v91
	v_div_fixup_f32 v89, v79, v78, 1.0
	v_mul_f32_e32 v3, v3, v89
	v_mul_f32_e32 v3, v3, v34
	v_mov_b32_e32 v90, v181
	v_cvt_pk_fp8_f32 v90, v3, 0
	v_ashrrev_i32_e32 v3, 31, v2
	v_lshlrev_b64 v[78:79], 10, v[2:3]
	v_mul_f32_e32 v3, v76, v89
	v_mul_f32_e32 v3, v3, v32
	v_mov_b32_e32 v76, v181
	v_lshl_add_u64 v[78:79], v[4:5], 0, v[78:79]
	v_cvt_pk_fp8_f32 v76, v3, 0
	v_mul_f32_e32 v3, v105, v89
	v_readfirstlane_b32 s100, v78
	v_readfirstlane_b32 s101, v79
	v_lshrrev_b32_e32 v239, 6, v0
	v_lshlrev_b32_e32 v239, 12, v239
	v_add_u32_e32 v239, 0x10000, v239
	v_and_b32_e32 v241, 63, v0
	v_and_b32_e32 v242, 31, v241
	v_lshrrev_b32_e32 v243, 5, v241
	v_lshl_add_u32 v242, v243, 9, v242
	v_add_u32_e32 v242, v239, v242
	v_lshrrev_b32_e32 v243, 3, v241
	v_lshlrev_b32_e32 v243, 10, v243
	v_and_b32_e32 v238, 7, v241
	v_lshl_add_u32 v243, v238, 4, v243
	v_lshl_add_u32 v241, v241, 4, v239
	v_mov_b32_e32 v238, v243
	v_mov_b32_e32 v239, 0
	v_lshl_add_u64 v[238:239], v[238:239], 0, s[100:101]
	ds_write_b8 v242, v90 offset:0
	v_mul_f32_e32 v3, v3, v31
	v_mov_b32_e32 v90, v181
	v_cvt_pk_fp8_f32 v90, v3, 0
	v_mul_f32_e32 v3, v82, v89
	v_mul_f32_e32 v82, 0x4f800000, v77
	v_cmp_gt_f32_e32 vcc, s55, v77
	v_mul_f32_e32 v3, v3, v30
	v_mov_b32_e32 v89, v181
	v_cndmask_b32_e32 v77, v77, v82, vcc
	v_sqrt_f32_e32 v82, v77
	v_cvt_pk_fp8_f32 v89, v3, 0
	ds_write_b8 v242, v76 offset:32
	ds_write_b8 v242, v90 offset:64
	ds_write_b8 v242, v89 offset:96
	v_add_u32_e32 v3, -1, v82
	v_fma_f32 v91, -v3, v82, v77
	v_cmp_ge_f32_e64 s[6:7], 0, v91
	v_add_u32_e32 v91, 1, v82
	s_xor_b32 s100, s98, 1
	s_and_b32 s100, s100, s99
	s_cselect_b32 s101, 0, s18
	s_mov_b32 s98, s100
	s_mov_b32 s99, 0
	s_add_i32 s53, s53, s101
	v_cndmask_b32_e64 v3, v82, v3, s[6:7]
	v_fma_f32 v82, -v91, v82, v77
	v_cmp_lt_f32_e64 s[6:7], 0, v82
	s_cmp_lt_i32 s53, s35
	s_nop 0
	v_cndmask_b32_e64 v3, v3, v91, s[6:7]
	v_mul_f32_e32 v82, 0x37800000, v3
	v_cndmask_b32_e32 v3, v3, v82, vcc
	v_cmp_class_f32_e32 vcc, v77, v185
	s_nop 1
	v_cndmask_b32_e32 v3, v3, v77, vcc
	v_div_scale_f32 v77, s[6:7], v3, v3, 1.0
	v_rcp_f32_e32 v82, v77
	s_nop 0
	v_fma_f32 v76, -v77, v82, 1.0
	v_fmac_f32_e32 v82, v76, v82
	v_div_scale_f32 v76, vcc, 1.0, v3, 1.0
	v_mul_f32_e32 v78, v76, v82
	v_fma_f32 v79, -v77, v78, v76
	v_fmac_f32_e32 v78, v79, v82
	v_fma_f32 v76, -v77, v78, v76
	v_div_fmas_f32 v76, v76, v82, v78
	v_div_fixup_f32 v3, v76, v3, 1.0
	v_mul_f32_e32 v68, v68, v3
	v_mul_f32_e32 v68, v68, v34
	v_mov_b32_e32 v78, v181
	v_or_b32_e32 v76, 1, v2
	v_cvt_pk_fp8_f32 v78, v68, 0
	v_ashrrev_i32_e32 v77, 31, v76
	v_mul_f32_e32 v68, v71, v3
	v_lshlrev_b64 v[76:77], 10, v[76:77]
	v_mul_f32_e32 v68, v68, v32
	v_mov_b32_e32 v71, v181
	v_lshl_add_u64 v[76:77], v[4:5], 0, v[76:77]
	v_cvt_pk_fp8_f32 v71, v68, 0
	v_mul_f32_e32 v68, v83, v3
	ds_write_b8 v242, v78 offset:128
	v_mul_f32_e32 v68, v68, v31
	v_mov_b32_e32 v78, v181
	v_cvt_pk_fp8_f32 v78, v68, 0
	v_fmamk_f32 v68, v80, 0x3c000000, v184
	v_mul_f32_e32 v79, 0x4f800000, v68
	v_cmp_gt_f32_e32 vcc, s55, v68
	v_mul_f32_e32 v3, v84, v3
	v_mul_f32_e32 v3, v3, v30
	v_cndmask_b32_e32 v68, v68, v79, vcc
	v_sqrt_f32_e32 v79, v68
	v_mov_b32_e32 v80, v181
	v_cvt_pk_fp8_f32 v80, v3, 0
	ds_write_b8 v242, v71 offset:160
	ds_write_b8 v242, v78 offset:192
	ds_write_b8 v242, v80 offset:224
	v_add_u32_e32 v3, -1, v79
	v_fma_f32 v82, -v3, v79, v68
	v_cmp_ge_f32_e64 s[6:7], 0, v82
	v_add_u32_e32 v82, 1, v79
	s_nop 0
	v_cndmask_b32_e64 v3, v79, v3, s[6:7]
	v_fma_f32 v79, -v82, v79, v68
	v_cmp_lt_f32_e64 s[6:7], 0, v79
	s_nop 1
	v_cndmask_b32_e64 v3, v3, v82, s[6:7]
	v_mul_f32_e32 v79, 0x37800000, v3
	v_cndmask_b32_e32 v3, v3, v79, vcc
	v_cmp_class_f32_e32 vcc, v68, v185
	s_nop 1
	v_cndmask_b32_e32 v3, v3, v68, vcc
	v_div_scale_f32 v68, s[6:7], v3, v3, 1.0
	v_rcp_f32_e32 v79, v68
	s_nop 0
	v_fma_f32 v71, -v68, v79, 1.0
	v_fmac_f32_e32 v79, v71, v79
	v_div_scale_f32 v71, vcc, 1.0, v3, 1.0
	v_mul_f32_e32 v76, v71, v79
	v_fma_f32 v77, -v68, v76, v71
	v_fmac_f32_e32 v76, v77, v79
	v_fma_f32 v68, -v68, v76, v71
	v_div_fmas_f32 v68, v68, v79, v76
	v_div_fixup_f32 v3, v68, v3, 1.0
	v_mul_f32_e32 v63, v63, v3
	v_mul_f32_e32 v63, v63, v34
	v_mov_b32_e32 v68, v181
	v_or_b32_e32 v76, 2, v2
	v_cvt_pk_fp8_f32 v68, v63, 0
	v_ashrrev_i32_e32 v77, 31, v76
	v_mul_f32_e32 v63, v66, v3
	v_lshlrev_b64 v[76:77], 10, v[76:77]
	v_mul_f32_e32 v63, v63, v32
	v_mov_b32_e32 v66, v181
	v_lshl_add_u64 v[76:77], v[4:5], 0, v[76:77]
	v_cvt_pk_fp8_f32 v66, v63, 0
	v_mul_f32_e32 v63, v73, v3
	ds_write_b8 v242, v68 offset:256
	v_mul_f32_e32 v63, v63, v31
	v_mov_b32_e32 v68, v181
	v_cvt_pk_fp8_f32 v68, v63, 0
	v_fmamk_f32 v63, v81, 0x3c000000, v184
	v_mul_f32_e32 v71, 0x4f800000, v63
	v_cmp_gt_f32_e32 vcc, s55, v63
	v_mul_f32_e32 v3, v87, v3
	v_mul_f32_e32 v3, v3, v30
	v_cndmask_b32_e32 v63, v63, v71, vcc
	v_sqrt_f32_e32 v71, v63
	v_mov_b32_e32 v73, v181
	v_cvt_pk_fp8_f32 v73, v3, 0
	ds_write_b8 v242, v66 offset:288
	ds_write_b8 v242, v68 offset:320
	ds_write_b8 v242, v73 offset:352
	v_add_u32_e32 v3, -1, v71
	v_fma_f32 v78, -v3, v71, v63
	v_cmp_ge_f32_e64 s[6:7], 0, v78
	v_add_u32_e32 v78, 1, v71
	v_or_b32_e32 v76, 3, v2
	v_cndmask_b32_e64 v3, v71, v3, s[6:7]
	v_fma_f32 v71, -v78, v71, v63
	v_cmp_lt_f32_e64 s[6:7], 0, v71
	v_ashrrev_i32_e32 v77, 31, v76
	v_lshlrev_b64 v[76:77], 10, v[76:77]
	v_cndmask_b32_e64 v3, v3, v78, s[6:7]
	v_mul_f32_e32 v71, 0x37800000, v3
	v_cndmask_b32_e32 v3, v3, v71, vcc
	v_cmp_class_f32_e32 vcc, v63, v185
	v_lshl_add_u64 v[76:77], v[4:5], 0, v[76:77]
	s_nop 0
	v_cndmask_b32_e32 v3, v3, v63, vcc
	v_div_scale_f32 v63, s[6:7], v3, v3, 1.0
	v_rcp_f32_e32 v71, v63
	s_nop 0
	v_fma_f32 v66, -v63, v71, 1.0
	v_fmac_f32_e32 v71, v66, v71
	v_div_scale_f32 v66, vcc, 1.0, v3, 1.0
	v_mul_f32_e32 v68, v66, v71
	v_fma_f32 v73, -v63, v68, v66
	v_fmac_f32_e32 v68, v73, v71
	v_fma_f32 v63, -v63, v68, v66
	v_div_fmas_f32 v63, v63, v71, v68
	v_div_fixup_f32 v3, v63, v3, 1.0
	v_mul_f32_e32 v58, v58, v3
	v_mul_f32_e32 v58, v58, v34
	v_mov_b32_e32 v63, v181
	v_cvt_pk_fp8_f32 v63, v58, 0
	v_mul_f32_e32 v58, v61, v3
	v_mul_f32_e32 v58, v58, v32
	v_mov_b32_e32 v61, v181
	v_cvt_pk_fp8_f32 v61, v58, 0
	v_mul_f32_e32 v58, v69, v3
	ds_write_b8 v242, v63 offset:384
	v_mul_f32_e32 v58, v58, v31
	v_mov_b32_e32 v63, v181
	v_cvt_pk_fp8_f32 v63, v58, 0
	v_fmamk_f32 v58, v85, 0x3c000000, v184
	v_mul_f32_e32 v66, 0x4f800000, v58
	v_cmp_gt_f32_e32 vcc, s55, v58
	v_mul_f32_e32 v3, v74, v3
	v_mul_f32_e32 v3, v3, v30
	v_cndmask_b32_e32 v58, v58, v66, vcc
	v_sqrt_f32_e32 v66, v58
	v_mov_b32_e32 v68, v181
	v_cvt_pk_fp8_f32 v68, v3, 0
	ds_write_b8 v242, v61 offset:416
	ds_write_b8 v242, v63 offset:448
	ds_write_b8 v242, v68 offset:480
	v_add_u32_e32 v3, -1, v66
	v_fma_f32 v69, -v3, v66, v58
	v_cmp_ge_f32_e64 s[6:7], 0, v69
	v_add_u32_e32 v69, 1, v66
	s_nop 0
	v_cndmask_b32_e64 v3, v66, v3, s[6:7]
	v_fma_f32 v66, -v69, v66, v58
	v_cmp_lt_f32_e64 s[6:7], 0, v66
	s_nop 1
	v_cndmask_b32_e64 v3, v3, v69, s[6:7]
	v_mul_f32_e32 v66, 0x37800000, v3
	v_cndmask_b32_e32 v3, v3, v66, vcc
	v_cmp_class_f32_e32 vcc, v58, v185
	s_nop 1
	v_cndmask_b32_e32 v3, v3, v58, vcc
	v_div_scale_f32 v58, s[6:7], v3, v3, 1.0
	v_rcp_f32_e32 v66, v58
	s_nop 0
	v_fma_f32 v61, -v58, v66, 1.0
	v_fmac_f32_e32 v66, v61, v66
	v_div_scale_f32 v61, vcc, 1.0, v3, 1.0
	v_mul_f32_e32 v63, v61, v66
	v_fma_f32 v68, -v58, v63, v61
	v_fmac_f32_e32 v63, v68, v66
	v_fma_f32 v58, -v58, v63, v61
	v_div_fmas_f32 v58, v58, v66, v63
	v_div_fixup_f32 v3, v58, v3, 1.0
	v_mul_f32_e32 v53, v53, v3
	v_mul_f32_e32 v53, v53, v34
	v_mov_b32_e32 v58, v181
	v_add_u32_e32 v68, 8, v2
	v_cvt_pk_fp8_f32 v58, v53, 0
	v_ashrrev_i32_e32 v69, 31, v68
	v_mul_f32_e32 v53, v56, v3
	v_lshlrev_b64 v[68:69], 10, v[68:69]
	v_mul_f32_e32 v53, v53, v32
	v_mov_b32_e32 v56, v181
	v_lshl_add_u64 v[68:69], v[4:5], 0, v[68:69]
	v_cvt_pk_fp8_f32 v56, v53, 0
	v_mul_f32_e32 v53, v64, v3
	ds_write_b8 v242, v58 offset:1024
	v_mul_f32_e32 v53, v53, v31
	v_mov_b32_e32 v58, v181
	v_cvt_pk_fp8_f32 v58, v53, 0
	v_fmamk_f32 v53, v86, 0x3c000000, v184
	v_mul_f32_e32 v61, 0x4f800000, v53
	v_cmp_gt_f32_e32 vcc, s55, v53
	v_mul_f32_e32 v3, v70, v3
	v_mul_f32_e32 v3, v3, v30
	v_cndmask_b32_e32 v53, v53, v61, vcc
	v_sqrt_f32_e32 v61, v53
	v_mov_b32_e32 v63, v181
	v_cvt_pk_fp8_f32 v63, v3, 0
	ds_write_b8 v242, v56 offset:1056
	ds_write_b8 v242, v58 offset:1088
	ds_write_b8 v242, v63 offset:1120
	v_add_u32_e32 v3, -1, v61
	v_fma_f32 v64, -v3, v61, v53
	v_cmp_ge_f32_e64 s[6:7], 0, v64
	v_add_u32_e32 v64, 1, v61
	v_add_u32_e32 v68, 9, v2
	v_cndmask_b32_e64 v3, v61, v3, s[6:7]
	v_fma_f32 v61, -v64, v61, v53
	v_cmp_lt_f32_e64 s[6:7], 0, v61
	v_ashrrev_i32_e32 v69, 31, v68
	v_lshlrev_b64 v[68:69], 10, v[68:69]
	v_cndmask_b32_e64 v3, v3, v64, s[6:7]
	v_mul_f32_e32 v61, 0x37800000, v3
	v_cndmask_b32_e32 v3, v3, v61, vcc
	v_cmp_class_f32_e32 vcc, v53, v185
	v_lshl_add_u64 v[68:69], v[4:5], 0, v[68:69]
	s_nop 0
	v_cndmask_b32_e32 v3, v3, v53, vcc
	v_div_scale_f32 v53, s[6:7], v3, v3, 1.0
	v_rcp_f32_e32 v61, v53
	s_nop 0
	v_fma_f32 v56, -v53, v61, 1.0
	v_fmac_f32_e32 v61, v56, v61
	v_div_scale_f32 v56, vcc, 1.0, v3, 1.0
	v_mul_f32_e32 v58, v56, v61
	v_fma_f32 v63, -v53, v58, v56
	v_fmac_f32_e32 v58, v63, v61
	v_fma_f32 v53, -v53, v58, v56
	v_div_fmas_f32 v53, v53, v61, v58
	v_div_fixup_f32 v3, v53, v3, 1.0
	v_mul_f32_e32 v47, v47, v3
	v_mul_f32_e32 v47, v47, v34
	v_mov_b32_e32 v53, v181
	v_cvt_pk_fp8_f32 v53, v47, 0
	v_mul_f32_e32 v47, v51, v3
	v_mul_f32_e32 v47, v47, v32
	v_mov_b32_e32 v51, v181
	v_cvt_pk_fp8_f32 v51, v47, 0
	v_mul_f32_e32 v47, v59, v3
	ds_write_b8 v242, v53 offset:1152
	v_mul_f32_e32 v47, v47, v31
	v_mov_b32_e32 v53, v181
	v_cvt_pk_fp8_f32 v53, v47, 0
	v_fmamk_f32 v47, v88, 0x3c000000, v184
	v_mul_f32_e32 v56, 0x4f800000, v47
	v_cmp_gt_f32_e32 vcc, s55, v47
	v_mul_f32_e32 v3, v65, v3
	v_mul_f32_e32 v3, v3, v30
	v_cndmask_b32_e32 v47, v47, v56, vcc
	v_sqrt_f32_e32 v56, v47
	v_mov_b32_e32 v58, v181
	v_cvt_pk_fp8_f32 v58, v3, 0
	ds_write_b8 v242, v51 offset:1184
	ds_write_b8 v242, v53 offset:1216
	ds_write_b8 v242, v58 offset:1248
	v_add_u32_e32 v3, -1, v56
	v_fma_f32 v59, -v3, v56, v47
	v_cmp_ge_f32_e64 s[6:7], 0, v59
	v_add_u32_e32 v59, 1, v56
	s_nop 0
	v_cndmask_b32_e64 v3, v56, v3, s[6:7]
	v_fma_f32 v56, -v59, v56, v47
	v_cmp_lt_f32_e64 s[6:7], 0, v56
	s_nop 1
	v_cndmask_b32_e64 v3, v3, v59, s[6:7]
	v_mul_f32_e32 v56, 0x37800000, v3
	v_cndmask_b32_e32 v3, v3, v56, vcc
	v_cmp_class_f32_e32 vcc, v47, v185
	s_nop 1
	v_cndmask_b32_e32 v3, v3, v47, vcc
	v_div_scale_f32 v47, s[6:7], v3, v3, 1.0
	v_rcp_f32_e32 v56, v47
	s_nop 0
	v_fma_f32 v51, -v47, v56, 1.0
	v_fmac_f32_e32 v56, v51, v56
	v_div_scale_f32 v51, vcc, 1.0, v3, 1.0
	v_mul_f32_e32 v53, v51, v56
	v_fma_f32 v58, -v47, v53, v51
	v_fmac_f32_e32 v53, v58, v56
	v_fma_f32 v47, -v47, v53, v51
	v_div_fmas_f32 v47, v47, v56, v53
	v_div_fixup_f32 v3, v47, v3, 1.0
	v_mul_f32_e32 v42, v42, v3
	v_mul_f32_e32 v42, v42, v34
	v_mov_b32_e32 v47, v181
	v_add_u32_e32 v58, 10, v2
	v_cvt_pk_fp8_f32 v47, v42, 0
	v_ashrrev_i32_e32 v59, 31, v58
	v_mul_f32_e32 v42, v46, v3
	v_lshlrev_b64 v[58:59], 10, v[58:59]
	v_mul_f32_e32 v42, v42, v32
	v_mov_b32_e32 v46, v181
	v_lshl_add_u64 v[58:59], v[4:5], 0, v[58:59]
	v_cvt_pk_fp8_f32 v46, v42, 0
	v_mul_f32_e32 v42, v54, v3
	ds_write_b8 v242, v47 offset:1280
	v_mul_f32_e32 v42, v42, v31
	v_mov_b32_e32 v47, v181
	v_cvt_pk_fp8_f32 v47, v42, 0
	v_fmamk_f32 v42, v75, 0x3c000000, v184
	v_mul_f32_e32 v51, 0x4f800000, v42
	v_cmp_gt_f32_e32 vcc, s55, v42
	v_mul_f32_e32 v3, v60, v3
	v_mul_f32_e32 v3, v3, v30
	v_cndmask_b32_e32 v42, v42, v51, vcc
	v_sqrt_f32_e32 v51, v42
	v_mov_b32_e32 v53, v181
	v_cvt_pk_fp8_f32 v53, v3, 0
	ds_write_b8 v242, v46 offset:1312
	ds_write_b8 v242, v47 offset:1344
	ds_write_b8 v242, v53 offset:1376
	v_add_u32_e32 v3, -1, v51
	v_fma_f32 v54, -v3, v51, v42
	v_cmp_ge_f32_e64 s[6:7], 0, v54
	v_add_u32_e32 v54, 1, v51
	s_nop 0
	v_cndmask_b32_e64 v3, v51, v3, s[6:7]
	v_fma_f32 v51, -v54, v51, v42
	v_cmp_lt_f32_e64 s[6:7], 0, v51
	s_nop 1
	v_cndmask_b32_e64 v3, v3, v54, s[6:7]
	v_mul_f32_e32 v51, 0x37800000, v3
	v_cndmask_b32_e32 v3, v3, v51, vcc
	v_cmp_class_f32_e32 vcc, v42, v185
	s_nop 1
	v_cndmask_b32_e32 v3, v3, v42, vcc
	v_div_scale_f32 v42, s[6:7], v3, v3, 1.0
	v_rcp_f32_e32 v51, v42
	s_nop 0
	v_fma_f32 v46, -v42, v51, 1.0
	v_fmac_f32_e32 v51, v46, v51
	v_div_scale_f32 v46, vcc, 1.0, v3, 1.0
	v_mul_f32_e32 v47, v46, v51
	v_fma_f32 v53, -v42, v47, v46
	v_fmac_f32_e32 v47, v53, v51
	v_fma_f32 v42, -v42, v47, v46
	v_div_fmas_f32 v42, v42, v51, v47
	v_div_fixup_f32 v3, v42, v3, 1.0
	v_mul_f32_e32 v36, v36, v3
	v_mul_f32_e32 v36, v36, v34
	v_mov_b32_e32 v42, v181
	v_add_u32_e32 v46, 11, v2
	v_cvt_pk_fp8_f32 v42, v36, 0
	v_ashrrev_i32_e32 v47, 31, v46
	v_mul_f32_e32 v36, v41, v3
	v_lshlrev_b64 v[46:47], 10, v[46:47]
	v_mul_f32_e32 v36, v36, v32
	v_mov_b32_e32 v41, v181
	v_lshl_add_u64 v[46:47], v[4:5], 0, v[46:47]
	v_cvt_pk_fp8_f32 v41, v36, 0
	v_mul_f32_e32 v36, v49, v3
	ds_write_b8 v242, v42 offset:1408
	v_mul_f32_e32 v36, v36, v31
	v_mov_b32_e32 v42, v181
	v_cvt_pk_fp8_f32 v42, v36, 0
	v_fmamk_f32 v36, v72, 0x3c000000, v184
	v_mul_f32_e32 v49, 0x4f800000, v36
	v_cmp_gt_f32_e32 vcc, s55, v36
	v_mul_f32_e32 v3, v55, v3
	v_mul_f32_e32 v3, v3, v30
	v_cndmask_b32_e32 v36, v36, v49, vcc
	v_sqrt_f32_e32 v49, v36
	v_mov_b32_e32 v51, v181
	v_cvt_pk_fp8_f32 v51, v3, 0
	ds_write_b8 v242, v41 offset:1440
	ds_write_b8 v242, v42 offset:1472
	ds_write_b8 v242, v51 offset:1504
	v_add_u32_e32 v3, -1, v49
	v_fma_f32 v53, -v3, v49, v36
	v_cmp_ge_f32_e64 s[6:7], 0, v53
	v_add_u32_e32 v53, 1, v49
	s_nop 0
	v_cndmask_b32_e64 v3, v49, v3, s[6:7]
	v_fma_f32 v49, -v53, v49, v36
	v_cmp_lt_f32_e64 s[6:7], 0, v49
	s_nop 1
	v_cndmask_b32_e64 v3, v3, v53, s[6:7]
	v_mul_f32_e32 v49, 0x37800000, v3
	v_cndmask_b32_e32 v3, v3, v49, vcc
	v_cmp_class_f32_e32 vcc, v36, v185
	s_nop 1
	v_cndmask_b32_e32 v3, v3, v36, vcc
	v_div_scale_f32 v36, s[6:7], v3, v3, 1.0
	v_rcp_f32_e32 v49, v36
	s_nop 0
	v_fma_f32 v41, -v36, v49, 1.0
	v_fmac_f32_e32 v49, v41, v49
	v_div_scale_f32 v41, vcc, 1.0, v3, 1.0
	v_mul_f32_e32 v42, v41, v49
	v_fma_f32 v46, -v36, v42, v41
	v_fmac_f32_e32 v42, v46, v49
	v_fma_f32 v36, -v36, v42, v41
	v_div_fmas_f32 v36, v36, v49, v42
	v_div_fixup_f32 v3, v36, v3, 1.0
	v_mul_f32_e32 v28, v28, v3
	v_mul_f32_e32 v28, v28, v34
	v_mov_b32_e32 v36, v181
	v_add_u32_e32 v46, 16, v2
	v_cvt_pk_fp8_f32 v36, v28, 0
	v_ashrrev_i32_e32 v47, 31, v46
	v_lshlrev_b64 v[46:47], 10, v[46:47]
	v_lshl_add_u64 v[46:47], v[4:5], 0, v[46:47]
	v_mul_f32_e32 v28, v37, v3
	ds_write_b8 v242, v36 offset:2048
	v_mul_f32_e32 v28, v28, v32
	v_mov_b32_e32 v36, v181
	v_cvt_pk_fp8_f32 v36, v28, 0
	v_mul_f32_e32 v28, v44, v3
	v_mul_f32_e32 v28, v28, v31
	v_mov_b32_e32 v37, v181
	v_cvt_pk_fp8_f32 v37, v28, 0
	v_fmamk_f32 v28, v67, 0x3c000000, v184
	v_mul_f32_e32 v41, 0x4f800000, v28
	v_cmp_gt_f32_e32 vcc, s55, v28
	v_mul_f32_e32 v3, v50, v3
	v_mul_f32_e32 v3, v3, v30
	v_cndmask_b32_e32 v28, v28, v41, vcc
	v_sqrt_f32_e32 v41, v28
	v_mov_b32_e32 v42, v181
	v_cvt_pk_fp8_f32 v42, v3, 0
	ds_write_b8 v242, v36 offset:2080
	ds_write_b8 v242, v37 offset:2112
	ds_write_b8 v242, v42 offset:2144
	v_add_u32_e32 v3, -1, v41
	v_fma_f32 v44, -v3, v41, v28
	v_cmp_ge_f32_e64 s[6:7], 0, v44
	v_add_u32_e32 v44, 1, v41
	s_nop 0
	v_cndmask_b32_e64 v3, v41, v3, s[6:7]
	v_fma_f32 v41, -v44, v41, v28
	v_cmp_lt_f32_e64 s[6:7], 0, v41
	s_nop 1
	v_cndmask_b32_e64 v3, v3, v44, s[6:7]
	v_mul_f32_e32 v41, 0x37800000, v3
	v_cndmask_b32_e32 v3, v3, v41, vcc
	v_cmp_class_f32_e32 vcc, v28, v185
	s_nop 1
	v_cndmask_b32_e32 v3, v3, v28, vcc
	v_div_scale_f32 v28, s[6:7], v3, v3, 1.0
	v_rcp_f32_e32 v41, v28
	s_nop 0
	v_fma_f32 v36, -v28, v41, 1.0
	v_fmac_f32_e32 v41, v36, v41
	v_div_scale_f32 v36, vcc, 1.0, v3, 1.0
	v_mul_f32_e32 v37, v36, v41
	v_fma_f32 v42, -v28, v37, v36
	v_fmac_f32_e32 v37, v42, v41
	v_fma_f32 v28, -v28, v37, v36
	v_div_fmas_f32 v28, v28, v41, v37
	v_div_fixup_f32 v3, v28, v3, 1.0
	v_mul_f32_e32 v24, v24, v3
	v_mul_f32_e32 v24, v24, v34
	v_mov_b32_e32 v28, v181
	v_add_u32_e32 v36, 17, v2
	v_cvt_pk_fp8_f32 v28, v24, 0
	v_ashrrev_i32_e32 v37, 31, v36
	v_lshlrev_b64 v[36:37], 10, v[36:37]
	v_lshl_add_u64 v[36:37], v[4:5], 0, v[36:37]
	v_mul_f32_e32 v24, v29, v3
	ds_write_b8 v242, v28 offset:2176
	v_mul_f32_e32 v24, v24, v32
	v_mov_b32_e32 v28, v181
	v_cvt_pk_fp8_f32 v28, v24, 0
	v_mul_f32_e32 v24, v39, v3
	v_mul_f32_e32 v24, v24, v31
	v_mov_b32_e32 v29, v181
	v_cvt_pk_fp8_f32 v29, v24, 0
	v_fmamk_f32 v24, v62, 0x3c000000, v184
	v_mul_f32_e32 v39, 0x4f800000, v24
	v_cmp_gt_f32_e32 vcc, s55, v24
	v_mul_f32_e32 v3, v45, v3
	v_mul_f32_e32 v3, v3, v30
	v_cndmask_b32_e32 v24, v24, v39, vcc
	v_sqrt_f32_e32 v39, v24
	v_mov_b32_e32 v41, v181
	v_cvt_pk_fp8_f32 v41, v3, 0
	ds_write_b8 v242, v28 offset:2208
	ds_write_b8 v242, v29 offset:2240
	ds_write_b8 v242, v41 offset:2272
	v_add_u32_e32 v3, -1, v39
	v_fma_f32 v42, -v3, v39, v24
	v_cmp_ge_f32_e64 s[6:7], 0, v42
	v_add_u32_e32 v42, 1, v39
	s_nop 0
	v_cndmask_b32_e64 v3, v39, v3, s[6:7]
	v_fma_f32 v39, -v42, v39, v24
	v_cmp_lt_f32_e64 s[6:7], 0, v39
	s_nop 1
	v_cndmask_b32_e64 v3, v3, v42, s[6:7]
	v_mul_f32_e32 v39, 0x37800000, v3
	v_cndmask_b32_e32 v3, v3, v39, vcc
	v_cmp_class_f32_e32 vcc, v24, v185
	s_nop 1
	v_cndmask_b32_e32 v3, v3, v24, vcc
	v_div_scale_f32 v24, s[6:7], v3, v3, 1.0
	v_rcp_f32_e32 v39, v24
	s_nop 0
	v_fma_f32 v28, -v24, v39, 1.0
	v_fmac_f32_e32 v39, v28, v39
	v_div_scale_f32 v28, vcc, 1.0, v3, 1.0
	v_mul_f32_e32 v29, v28, v39
	v_fma_f32 v36, -v24, v29, v28
	v_fmac_f32_e32 v29, v36, v39
	v_fma_f32 v24, -v24, v29, v28
	v_div_fmas_f32 v24, v24, v39, v29
	v_div_fixup_f32 v3, v24, v3, 1.0
	v_mul_f32_e32 v20, v20, v3
	v_mul_f32_e32 v20, v20, v34
	v_mov_b32_e32 v24, v181
	v_add_u32_e32 v28, 18, v2
	v_cvt_pk_fp8_f32 v24, v20, 0
	v_ashrrev_i32_e32 v29, 31, v28
	v_lshlrev_b64 v[28:29], 10, v[28:29]
	v_lshl_add_u64 v[28:29], v[4:5], 0, v[28:29]
	v_mul_f32_e32 v20, v25, v3
	ds_write_b8 v242, v24 offset:2304
	v_mul_f32_e32 v20, v20, v32
	v_mov_b32_e32 v24, v181
	v_cvt_pk_fp8_f32 v24, v20, 0
	v_mul_f32_e32 v20, v33, v3
	v_mul_f32_e32 v20, v20, v31
	v_mov_b32_e32 v25, v181
	v_cvt_pk_fp8_f32 v25, v20, 0
	v_fmamk_f32 v20, v57, 0x3c000000, v184
	v_mul_f32_e32 v33, 0x4f800000, v20
	v_cmp_gt_f32_e32 vcc, s55, v20
	v_mul_f32_e32 v3, v40, v3
	v_mul_f32_e32 v3, v3, v30
	v_cndmask_b32_e32 v20, v20, v33, vcc
	v_sqrt_f32_e32 v33, v20
	v_mov_b32_e32 v36, v181
	v_cvt_pk_fp8_f32 v36, v3, 0
	ds_write_b8 v242, v24 offset:2336
	ds_write_b8 v242, v25 offset:2368
	ds_write_b8 v242, v36 offset:2400
	v_add_u32_e32 v3, -1, v33
	v_fma_f32 v37, -v3, v33, v20
	v_cmp_ge_f32_e64 s[6:7], 0, v37
	v_add_u32_e32 v37, 1, v33
	s_nop 0
	v_cndmask_b32_e64 v3, v33, v3, s[6:7]
	v_fma_f32 v33, -v37, v33, v20
	v_cmp_lt_f32_e64 s[6:7], 0, v33
	s_nop 1
	v_cndmask_b32_e64 v3, v3, v37, s[6:7]
	v_mul_f32_e32 v33, 0x37800000, v3
	v_cndmask_b32_e32 v3, v3, v33, vcc
	v_cmp_class_f32_e32 vcc, v20, v185
	s_nop 1
	v_cndmask_b32_e32 v3, v3, v20, vcc
	v_div_scale_f32 v20, s[6:7], v3, v3, 1.0
	v_rcp_f32_e32 v33, v20
	s_nop 0
	v_fma_f32 v24, -v20, v33, 1.0
	v_fmac_f32_e32 v33, v24, v33
	v_div_scale_f32 v24, vcc, 1.0, v3, 1.0
	v_mul_f32_e32 v25, v24, v33
	v_fma_f32 v28, -v20, v25, v24
	v_fmac_f32_e32 v25, v28, v33
	v_fma_f32 v20, -v20, v25, v24
	v_div_fmas_f32 v20, v20, v33, v25
	v_div_fixup_f32 v3, v20, v3, 1.0
	v_mul_f32_e32 v16, v16, v3
	v_mul_f32_e32 v16, v16, v34
	v_mov_b32_e32 v20, v181
	v_add_u32_e32 v24, 19, v2
	v_cvt_pk_fp8_f32 v20, v16, 0
	v_ashrrev_i32_e32 v25, 31, v24
	v_lshlrev_b64 v[24:25], 10, v[24:25]
	v_lshl_add_u64 v[24:25], v[4:5], 0, v[24:25]
	v_mul_f32_e32 v16, v21, v3
	ds_write_b8 v242, v20 offset:2432
	v_mul_f32_e32 v16, v16, v32
	v_mov_b32_e32 v20, v181
	v_cvt_pk_fp8_f32 v20, v16, 0
	v_mul_f32_e32 v16, v26, v3
	v_mul_f32_e32 v16, v16, v31
	v_mov_b32_e32 v21, v181
	v_cvt_pk_fp8_f32 v21, v16, 0
	v_fmamk_f32 v16, v52, 0x3c000000, v184
	v_mul_f32_e32 v26, 0x4f800000, v16
	v_cmp_gt_f32_e32 vcc, s55, v16
	v_mul_f32_e32 v3, v35, v3
	v_mul_f32_e32 v3, v3, v30
	v_cndmask_b32_e32 v16, v16, v26, vcc
	v_sqrt_f32_e32 v26, v16
	v_mov_b32_e32 v28, v181
	v_cvt_pk_fp8_f32 v28, v3, 0
	ds_write_b8 v242, v20 offset:2464
	ds_write_b8 v242, v21 offset:2496
	ds_write_b8 v242, v28 offset:2528
	v_add_u32_e32 v3, -1, v26
	v_fma_f32 v29, -v3, v26, v16
	v_cmp_ge_f32_e64 s[6:7], 0, v29
	v_add_u32_e32 v29, 1, v26
	s_nop 0
	v_cndmask_b32_e64 v3, v26, v3, s[6:7]
	v_fma_f32 v26, -v29, v26, v16
	v_cmp_lt_f32_e64 s[6:7], 0, v26
	s_nop 1
	v_cndmask_b32_e64 v3, v3, v29, s[6:7]
	v_mul_f32_e32 v26, 0x37800000, v3
	v_cndmask_b32_e32 v3, v3, v26, vcc
	v_cmp_class_f32_e32 vcc, v16, v185
	s_nop 1
	v_cndmask_b32_e32 v3, v3, v16, vcc
	v_div_scale_f32 v16, s[6:7], v3, v3, 1.0
	v_rcp_f32_e32 v26, v16
	s_nop 0
	v_fma_f32 v20, -v16, v26, 1.0
	v_fmac_f32_e32 v26, v20, v26
	v_div_scale_f32 v20, vcc, 1.0, v3, 1.0
	v_mul_f32_e32 v21, v20, v26
	v_fma_f32 v24, -v16, v21, v20
	v_fmac_f32_e32 v21, v24, v26
	v_fma_f32 v16, -v16, v21, v20
	v_div_fmas_f32 v16, v16, v26, v21
	v_div_fixup_f32 v3, v16, v3, 1.0
	v_mul_f32_e32 v12, v12, v3
	v_mul_f32_e32 v12, v12, v34
	v_mov_b32_e32 v16, v181
	v_add_u32_e32 v20, 24, v2
	v_cvt_pk_fp8_f32 v16, v12, 0
	v_ashrrev_i32_e32 v21, 31, v20
	v_lshlrev_b64 v[20:21], 10, v[20:21]
	v_lshl_add_u64 v[20:21], v[4:5], 0, v[20:21]
	v_mul_f32_e32 v12, v17, v3
	ds_write_b8 v242, v16 offset:3072
	v_mul_f32_e32 v12, v12, v32
	v_mov_b32_e32 v16, v181
	v_cvt_pk_fp8_f32 v16, v12, 0
	v_mul_f32_e32 v12, v22, v3
	v_mul_f32_e32 v12, v12, v31
	v_mov_b32_e32 v17, v181
	v_cvt_pk_fp8_f32 v17, v12, 0
	v_fmamk_f32 v12, v48, 0x3c000000, v184
	v_mul_f32_e32 v22, 0x4f800000, v12
	v_cmp_gt_f32_e32 vcc, s55, v12
	v_mul_f32_e32 v3, v27, v3
	v_mul_f32_e32 v3, v3, v30
	v_cndmask_b32_e32 v12, v12, v22, vcc
	v_sqrt_f32_e32 v22, v12
	v_mov_b32_e32 v24, v181
	v_cvt_pk_fp8_f32 v24, v3, 0
	ds_write_b8 v242, v16 offset:3104
	ds_write_b8 v242, v17 offset:3136
	ds_write_b8 v242, v24 offset:3168
	v_add_u32_e32 v3, -1, v22
	v_fma_f32 v25, -v3, v22, v12
	v_cmp_ge_f32_e64 s[6:7], 0, v25
	v_add_u32_e32 v25, 1, v22
	s_nop 0
	v_cndmask_b32_e64 v3, v22, v3, s[6:7]
	v_fma_f32 v22, -v25, v22, v12
	v_cmp_lt_f32_e64 s[6:7], 0, v22
	s_nop 1
	v_cndmask_b32_e64 v3, v3, v25, s[6:7]
	v_mul_f32_e32 v22, 0x37800000, v3
	v_cndmask_b32_e32 v3, v3, v22, vcc
	v_cmp_class_f32_e32 vcc, v12, v185
	s_nop 1
	v_cndmask_b32_e32 v3, v3, v12, vcc
	v_div_scale_f32 v12, s[6:7], v3, v3, 1.0
	v_rcp_f32_e32 v22, v12
	s_nop 0
	v_fma_f32 v16, -v12, v22, 1.0
	v_fmac_f32_e32 v22, v16, v22
	v_div_scale_f32 v16, vcc, 1.0, v3, 1.0
	v_mul_f32_e32 v17, v16, v22
	v_fma_f32 v20, -v12, v17, v16
	v_fmac_f32_e32 v17, v20, v22
	v_fma_f32 v12, -v12, v17, v16
	v_div_fmas_f32 v12, v12, v22, v17
	v_div_fixup_f32 v3, v12, v3, 1.0
	v_mul_f32_e32 v9, v9, v3
	v_mul_f32_e32 v9, v9, v34
	v_mov_b32_e32 v12, v181
	v_add_u32_e32 v16, 25, v2
	v_cvt_pk_fp8_f32 v12, v9, 0
	v_ashrrev_i32_e32 v17, 31, v16
	v_lshlrev_b64 v[16:17], 10, v[16:17]
	v_lshl_add_u64 v[16:17], v[4:5], 0, v[16:17]
	v_mul_f32_e32 v9, v13, v3
	ds_write_b8 v242, v12 offset:3200
	v_mul_f32_e32 v9, v9, v32
	v_mov_b32_e32 v12, v181
	v_cvt_pk_fp8_f32 v12, v9, 0
	v_mul_f32_e32 v9, v18, v3
	v_mul_f32_e32 v9, v9, v31
	v_mov_b32_e32 v13, v181
	v_cvt_pk_fp8_f32 v13, v9, 0
	v_fmamk_f32 v9, v43, 0x3c000000, v184
	v_mul_f32_e32 v18, 0x4f800000, v9
	v_cmp_gt_f32_e32 vcc, s55, v9
	v_mul_f32_e32 v3, v23, v3
	v_mul_f32_e32 v3, v3, v30
	v_cndmask_b32_e32 v9, v9, v18, vcc
	v_sqrt_f32_e32 v18, v9
	v_mov_b32_e32 v20, v181
	v_cvt_pk_fp8_f32 v20, v3, 0
	ds_write_b8 v242, v12 offset:3232
	ds_write_b8 v242, v13 offset:3264
	ds_write_b8 v242, v20 offset:3296
	v_add_u32_e32 v3, -1, v18
	v_fma_f32 v21, -v3, v18, v9
	v_cmp_ge_f32_e64 s[6:7], 0, v21
	v_add_u32_e32 v21, 1, v18
	s_nop 0
	v_cndmask_b32_e64 v3, v18, v3, s[6:7]
	v_fma_f32 v18, -v21, v18, v9
	v_cmp_lt_f32_e64 s[6:7], 0, v18
	s_nop 1
	v_cndmask_b32_e64 v3, v3, v21, s[6:7]
	v_mul_f32_e32 v18, 0x37800000, v3
	v_cndmask_b32_e32 v3, v3, v18, vcc
	v_cmp_class_f32_e32 vcc, v9, v185
	s_nop 1
	v_cndmask_b32_e32 v3, v3, v9, vcc
	v_div_scale_f32 v9, s[6:7], v3, v3, 1.0
	v_rcp_f32_e32 v18, v9
	s_nop 0
	v_fma_f32 v12, -v9, v18, 1.0
	v_fmac_f32_e32 v18, v12, v18
	v_div_scale_f32 v12, vcc, 1.0, v3, 1.0
	v_mul_f32_e32 v13, v12, v18
	v_fma_f32 v16, -v9, v13, v12
	v_fmac_f32_e32 v13, v16, v18
	v_fma_f32 v9, -v9, v13, v12
	v_div_fmas_f32 v9, v9, v18, v13
	v_div_fixup_f32 v3, v9, v3, 1.0
	v_mul_f32_e32 v7, v7, v3
	v_mul_f32_e32 v7, v7, v34
	v_mov_b32_e32 v9, v181
	v_add_u32_e32 v12, 26, v2
	v_cvt_pk_fp8_f32 v9, v7, 0
	v_ashrrev_i32_e32 v13, 31, v12
	v_lshlrev_b64 v[12:13], 10, v[12:13]
	v_lshl_add_u64 v[12:13], v[4:5], 0, v[12:13]
	v_mul_f32_e32 v7, v10, v3
	ds_write_b8 v242, v9 offset:3328
	v_mul_f32_e32 v7, v7, v32
	v_mov_b32_e32 v9, v181
	v_cvt_pk_fp8_f32 v9, v7, 0
	v_mul_f32_e32 v7, v14, v3
	v_mul_f32_e32 v7, v7, v31
	v_mov_b32_e32 v10, v181
	v_cvt_pk_fp8_f32 v10, v7, 0
	v_fmamk_f32 v7, v38, 0x3c000000, v184
	v_mul_f32_e32 v14, 0x4f800000, v7
	v_cmp_gt_f32_e32 vcc, s55, v7
	v_mul_f32_e32 v3, v19, v3
	v_mul_f32_e32 v3, v3, v30
	v_cndmask_b32_e32 v7, v7, v14, vcc
	v_sqrt_f32_e32 v14, v7
	v_mov_b32_e32 v16, v181
	v_cvt_pk_fp8_f32 v16, v3, 0
	ds_write_b8 v242, v9 offset:3360
	ds_write_b8 v242, v10 offset:3392
	ds_write_b8 v242, v16 offset:3424
	v_add_u32_e32 v3, -1, v14
	v_fma_f32 v17, -v3, v14, v7
	v_cmp_ge_f32_e64 s[6:7], 0, v17
	v_add_u32_e32 v17, 1, v14
	v_add_u32_e32 v2, 27, v2
	v_cndmask_b32_e64 v3, v14, v3, s[6:7]
	v_fma_f32 v14, -v17, v14, v7
	v_cmp_lt_f32_e64 s[6:7], 0, v14
	s_nop 1
	v_cndmask_b32_e64 v3, v3, v17, s[6:7]
	v_mul_f32_e32 v14, 0x37800000, v3
	v_cndmask_b32_e32 v3, v3, v14, vcc
	v_cmp_class_f32_e32 vcc, v7, v185
	s_nop 1
	v_cndmask_b32_e32 v3, v3, v7, vcc
	v_div_scale_f32 v7, s[6:7], v3, v3, 1.0
	v_rcp_f32_e32 v14, v7
	s_nop 0
	v_fma_f32 v9, -v7, v14, 1.0
	v_fmac_f32_e32 v14, v9, v14
	v_div_scale_f32 v9, vcc, 1.0, v3, 1.0
	v_mul_f32_e32 v10, v9, v14
	v_fma_f32 v12, -v7, v10, v9
	v_fmac_f32_e32 v10, v12, v14
	v_fma_f32 v7, -v7, v10, v9
	v_div_fmas_f32 v7, v7, v14, v10
	v_div_fixup_f32 v7, v7, v3, 1.0
	v_ashrrev_i32_e32 v3, 31, v2
	v_mul_f32_e32 v6, v6, v7
	v_lshlrev_b64 v[2:3], 10, v[2:3]
	v_mul_f32_e32 v6, v34, v6
	v_mov_b32_e32 v9, v181
	v_lshl_add_u64 v[2:3], v[4:5], 0, v[2:3]
	v_mul_f32_e32 v4, v11, v7
	v_cvt_pk_fp8_f32 v9, v6, 0
	v_mul_f32_e32 v6, v8, v7
	v_mul_f32_e32 v4, v31, v4
	v_mov_b32_e32 v5, v181
	v_mul_f32_e32 v6, v32, v6
	v_mov_b32_e32 v8, v181
	v_cvt_pk_fp8_f32 v5, v4, 0
	v_mul_f32_e32 v4, v15, v7
	v_cvt_pk_fp8_f32 v8, v6, 0
	v_mul_f32_e32 v4, v30, v4
	v_mov_b32_e32 v6, v181
	v_cvt_pk_fp8_f32 v6, v4, 0
	ds_write_b8 v242, v9 offset:3456
	ds_write_b8 v242, v8 offset:3488
	ds_write_b8 v242, v5 offset:3520
	ds_write_b8 v242, v6 offset:3552
	s_waitcnt lgkmcnt(0)
	s_mov_b32 s100, 0x2000
	s_mov_b32 s101, 0
	ds_read_b128 v[234:237], v241
	s_waitcnt lgkmcnt(0)
	global_store_dwordx4 v[238:239], v[234:237], off
	v_lshl_add_u64 v[238:239], v[238:239], 0, s[100:101]
	s_nop 1
	ds_read_b128 v[234:237], v241 offset:1024
	s_waitcnt lgkmcnt(0)
	global_store_dwordx4 v[238:239], v[234:237], off
	v_lshl_add_u64 v[238:239], v[238:239], 0, s[100:101]
	s_nop 1
	ds_read_b128 v[234:237], v241 offset:2048
	s_waitcnt lgkmcnt(0)
	global_store_dwordx4 v[238:239], v[234:237], off
	v_lshl_add_u64 v[238:239], v[238:239], 0, s[100:101]
	s_nop 1
	ds_read_b128 v[234:237], v241 offset:3072
	s_waitcnt lgkmcnt(0)
	global_store_dwordx4 v[238:239], v[234:237], off
	v_lshl_add_u64 v[238:239], v[238:239], 0, s[100:101]
	s_nop 1
	s_cbranch_scc0 .LBB0_1427
